# v64 + cache policy: thin-pass loads of y and h marked nt (stores unchanged)
# speedup vs baseline: 1.0048x; 1.0048x over previous
; __device__ __forceinline__ void thin_pass(const Ctx& C, const bf16* hin, bf16* hout, bf16* u, float* out, const bf16* y, const float* gpost, float cmul, const float* gpre, bool last) {
;     ...
;     for (int m0 = mstart; m0 < mend; m0 += mstep) {
;         v4u yr[RB][2], hr[RB][2];
; #pragma unroll
;         for (int b = 0; b < RB; ++b) { const v4u* yp = (const v4u*)(y + (size_t)(m0 + b) * D); const v4u* hp = (const v4u*)(hin + (size_t)(m0 + b) * D);
;             yr[b][0] = yp[lane]; yr[b][1] = yp[64 + lane]; hr[b][0] = hp[lane]; hr[b][1] = hp[64 + lane]; }
; #pragma unroll
;         for (int b = 0; b < RB; ++b) {
;             const int m = m0 + b; const v4u y0 = yr[b][0], y1 = yr[b][1], h0 = hr[b][0], h1 = hr[b][1];
;             f32x4 yv[4], h[4];
;             yv[0] = (f32x4){bf_lo(y0.x), bf_hi(y0.x), bf_lo(y0.y), bf_hi(y0.y)}; yv[1] = (f32x4){bf_lo(y0.z), bf_hi(y0.z), bf_lo(y0.w), bf_hi(y0.w)};
;             yv[2] = (f32x4){bf_lo(y1.x), bf_hi(y1.x), bf_lo(y1.y), bf_hi(y1.y)}; yv[3] = (f32x4){bf_lo(y1.z), bf_hi(y1.z), bf_lo(y1.w), bf_hi(y1.w)};
;             h[0] = (f32x4){bf_lo(h0.x), bf_hi(h0.x), bf_lo(h0.y), bf_hi(h0.y)}; h[1] = (f32x4){bf_lo(h0.z), bf_hi(h0.z), bf_lo(h0.w), bf_hi(h0.w)};
;             h[2] = (f32x4){bf_lo(h1.x), bf_hi(h1.x), bf_lo(h1.y), bf_hi(h1.y)}; h[3] = (f32x4){bf_lo(h1.z), bf_hi(h1.z), bf_lo(h1.w), bf_hi(h1.w)};
;             float ss = 0.f;
; #pragma unroll
;             for (int i = 0; i < 4; ++i) ss += (yv[i][0] * yv[i][0] + yv[i][1] * yv[i][1]) + (yv[i][2] * yv[i][2] + yv[i][3] * yv[i][3]);
;             const float ry = cmul / sqrtf(wave_sum(ss) * (1.0f / D) + RMS_EPS);
; #pragma unroll
;             for (int i = 0; i < 4; ++i) h[i] = h[i] + yv[i] * ry * g4[i];
.LBB0_734:
	v_lshl_add_u64 v[114:115], s[14:15], 0, v[100:101]
	v_add_co_u32_e32 v38, vcc, 0xd000000, v114
	v_lshl_add_u64 v[36:37], s[20:21], 0, v[100:101]
	s_nop 0
	v_addc_co_u32_e32 v39, vcc, 0, v115, vcc
	flat_load_dwordx4 v[84:87], v[36:37] nt
	flat_load_dwordx4 v[88:91], v[36:37] offset:1024 nt
	flat_load_dwordx4 v[92:95], v[38:39] offset:1024 nt
	flat_load_dwordx4 v[96:99], v[38:39] nt
	s_add_i32 s22, s10, 3
	flat_load_dwordx4 v[80:83], v[36:37] offset:2048 nt
	flat_load_dwordx4 v[68:71], v[36:37] offset:3072 nt
	v_add_co_u32_e32 v36, vcc, s84, v36
	s_ashr_i32 s23, s22, 31
	s_nop 0
	v_addc_co_u32_e32 v37, vcc, 0, v37, vcc
	v_add_co_u32_e32 v56, vcc, s91, v114
	s_lshl_b64 s[2:3], s[22:23], 11
	flat_load_dwordx4 v[64:67], v[36:37] nt
	flat_load_dwordx4 v[52:55], v[36:37] offset:1024 nt
	v_lshl_add_u64 v[36:37], v[102:103], 0, s[2:3]
	v_lshl_add_u64 v[58:59], v[104:105], 0, s[2:3]
	v_addc_co_u32_e32 v57, vcc, 0, v115, vcc
	flat_load_dwordx4 v[76:79], v[38:39] offset:2048 nt
	flat_load_dwordx4 v[72:75], v[38:39] offset:3072 nt
	flat_load_dwordx4 v[44:47], v[36:37] nt
	flat_load_dwordx4 v[40:43], v[36:37] offset:1024 nt
	flat_load_dwordx4 v[48:51], v[58:59] nt
	s_nop 0
	flat_load_dwordx4 v[36:39], v[58:59] offset:1024 nt
	flat_load_dwordx4 v[60:63], v[56:57] nt
	s_nop 0
	flat_load_dwordx4 v[56:59], v[56:57] offset:1024 nt
	s_waitcnt vmcnt(0) lgkmcnt(0)
	v_lshlrev_b32_e32 v118, 16, v86
	v_and_b32_e32 v119, 0xffff0000, v86
	v_lshlrev_b32_e32 v124, 16, v94
	v_and_b32_e32 v142, 0xffff0000, v94
	v_lshlrev_b32_e32 v86, 16, v96
	v_lshlrev_b32_e32 v94, 16, v97
	v_lshlrev_b32_e32 v120, 16, v87
	v_and_b32_e32 v121, 0xffff0000, v87
	v_lshlrev_b32_e32 v122, 16, v88
	v_and_b32_e32 v123, 0xffff0000, v88
	v_lshlrev_b32_e32 v126, 16, v95
	v_and_b32_e32 v127, 0xffff0000, v95
	v_and_b32_e32 v87, 0xffff0000, v96
	v_and_b32_e32 v95, 0xffff0000, v97
	v_lshlrev_b32_e32 v97, 16, v99
	v_lshlrev_b32_e32 v96, 16, v98
	v_and_b32_e32 v99, 0xffff0000, v99
	v_and_b32_e32 v98, 0xffff0000, v98
	v_mul_f32_e32 v2, v86, v86
	v_mul_f32_e32 v88, v94, v94
	v_lshlrev_b32_e32 v128, 16, v92
	v_and_b32_e32 v129, 0xffff0000, v92
	v_lshlrev_b32_e32 v92, 16, v93
	v_pk_mul_f32 v[130:131], v[98:99], v[98:99]
	v_pk_fma_f32 v[138:139], v[86:87], v[86:87], v[2:3] op_sel_hi:[1,1,0]
	v_pk_fma_f32 v[140:141], v[94:95], v[94:95], v[88:89] op_sel_hi:[1,1,0]
	v_and_b32_e32 v93, 0xffff0000, v93
	v_mul_f32_e32 v132, v128, v128
	v_mul_f32_e32 v134, v92, v92
	v_mov_b32_e32 v136, v124
	v_pk_fma_f32 v[130:131], v[96:97], v[96:97], v[130:131]
	v_mov_b32_e32 v125, v139
	v_mov_b32_e32 v137, v141
	v_pk_fma_f32 v[132:133], v[128:129], v[128:129], v[132:133] op_sel_hi:[1,1,0]
	v_pk_fma_f32 v[134:135], v[92:93], v[92:93], v[134:135] op_sel_hi:[1,1,0]
	v_pk_add_f32 v[130:131], v[130:131], v[130:131] op_sel_hi:[0,1]
	v_pk_add_f32 v[138:139], v[138:139], v[140:141]
	v_pk_mul_f32 v[136:137], v[124:125], v[136:137]
	v_mul_f32_e32 v132, v126, v126
	v_mul_f32_e32 v134, v127, v127
	v_mul_f32_e32 v130, v142, v142
	v_mov_b32_e32 v137, v139
	v_pk_add_f32 v[132:133], v[132:133], v[134:135]
	v_pk_add_f32 v[130:131], v[136:137], v[130:131]
	v_lshlrev_b32_e32 v134, 16, v91
	v_pk_add_f32 v[130:131], v[130:131], v[132:133]
	v_lshlrev_b32_e32 v132, 16, v90
	v_add_f32_e32 v2, v130, v131
	v_and_b32_e32 v135, 0xffff0000, v91
	v_lshlrev_b32_e32 v116, 16, v84
	v_add_f32_dpp v2, v2, v2 quad_perm:[1,0,3,2] row_mask:0xf bank_mask:0xf bound_ctrl:1
	v_and_b32_e32 v117, 0xffff0000, v84
	v_lshlrev_b32_e32 v84, 16, v85
	v_add_f32_dpp v2, v2, v2 quad_perm:[2,3,0,1] row_mask:0xf bank_mask:0xf bound_ctrl:1
	v_and_b32_e32 v85, 0xffff0000, v85
	s_nop 0
	v_add_f32_dpp v2, v2, v2 row_half_mirror row_mask:0xf bank_mask:0xf bound_ctrl:1
	s_nop 1
	v_add_f32_dpp v2, v2, v2 row_mirror row_mask:0xf bank_mask:0xf bound_ctrl:1
	s_nop 0
	v_readlane_b32 s1, v2, 16
	v_readlane_b32 s4, v2, 48
	v_readlane_b32 s2, v2, 0
	v_readlane_b32 s3, v2, 32
	v_mov_b32_e32 v130, s1
	v_mov_b32_e32 v131, s4
	v_pk_add_f32 v[130:131], s[2:3], v[130:131]
	s_mov_b64 s[4:5], -1
	v_add_f32_e32 v2, v130, v131
	v_fmamk_f32 v2, v2, 0x3a800000, v214
	v_lshlrev_b32_e32 v130, 16, v89
	v_and_b32_e32 v131, 0xffff0000, v89
	v_and_b32_e32 v133, 0xffff0000, v90
	v_rsq_f32_e32 v2, v2
	s_nop 0
	v_mul_f32_e32 v2, 0.5, v2
	v_pk_mul_f32 v[88:89], v[2:3], v[86:87] op_sel_hi:[0,1]
	v_pk_mul_f32 v[86:87], v[2:3], v[94:95] op_sel_hi:[0,1]
	v_pk_fma_f32 v[86:87], v[10:11], v[86:87], v[84:85]
	v_pk_fma_f32 v[84:85], v[8:9], v[88:89], v[116:117]
	v_mov_b32_e32 v88, v96
	v_mov_b32_e32 v89, v98
	v_mov_b32_e32 v98, v97
	v_pk_mul_f32 v[96:97], v[2:3], v[128:129] op_sel_hi:[0,1]
	v_pk_mul_f32 v[92:93], v[2:3], v[92:93] op_sel_hi:[0,1]
	v_mov_b32_e32 v125, v142
	v_pk_mul_f32 v[88:89], v[2:3], v[88:89] op_sel_hi:[0,1]
	v_pk_mul_f32 v[90:91], v[2:3], v[98:99] op_sel_hi:[0,1]
	v_pk_fma_f32 v[94:95], v[18:19], v[92:93], v[130:131]
	v_pk_fma_f32 v[92:93], v[16:17], v[96:97], v[122:123]
	v_pk_mul_f32 v[96:97], v[124:125], v[2:3] op_sel_hi:[1,0]
	v_pk_mul_f32 v[98:99], v[126:127], v[2:3] op_sel_hi:[1,0]
	v_cndmask_b32_e64 v2, 0, 1, s[6:7]
	v_pk_fma_f32 v[90:91], v[6:7], v[90:91], v[120:121]
	v_pk_fma_f32 v[88:89], v[4:5], v[88:89], v[118:119]
	v_pk_fma_f32 v[98:99], v[14:15], v[98:99], v[134:135]
	v_pk_fma_f32 v[96:97], v[12:13], v[96:97], v[132:133]
	v_cmp_ne_u32_e64 s[2:3], 1, v2
	s_andn2_b64 vcc, exec, s[6:7]
	v_lshl_add_u64 v[116:117], s[18:19], 0, v[100:101]
	s_cbranch_vccnz .LBB0_736
; __device__ __forceinline__ unsigned pk2(float lo, float hi) { unsigned r; asm("v_cvt_pk_bf16_f32 %0, %1, %2" : "=v"(r) : "v"(lo), "v"(hi)); return r; }
; __device__ __forceinline__ void thin_pass(const Ctx& C, const bf16* hin, bf16* hout, bf16* u, float* out, const bf16* y, const float* gpost, float cmul, const float* gpre, bool last) {
;     ...
;             else {
;                 float s2 = 0.f;
; #pragma unroll
;                 for (int i = 0; i < 4; ++i) s2 += (h[i][0] * h[i][0] + h[i][1] * h[i][1]) + (h[i][2] * h[i][2] + h[i][3] * h[i][3]);
;                 const float rh = 1.0f / sqrtf(wave_sum(s2) * (1.0f / D) + RMS_EPS);
;                 v4u o0, o1; o0.x = pk2(h[0][0], h[0][1]); o0.y = pk2(h[0][2], h[0][3]); o0.z = pk2(h[1][0], h[1][1]); o0.w = pk2(h[1][2], h[1][3]);
;                 o1.x = pk2(h[2][0], h[2][1]); o1.y = pk2(h[2][2], h[2][3]); o1.z = pk2(h[3][0], h[3][1]); o1.w = pk2(h[3][2], h[3][3]);
;                 v4u* hp = (v4u*)(hout + (size_t)m * D); hp[lane] = o0; hp[64 + lane] = o1;
; #pragma unroll
;                 for (int i = 0; i < 4; ++i) h[i] = h[i] * rh * q4[i];
;                 o0.x = pk2(h[0][0], h[0][1]); o0.y = pk2(h[0][2], h[0][3]); o0.z = pk2(h[1][0], h[1][1]); o0.w = pk2(h[1][2], h[1][3]);
;                 o1.x = pk2(h[2][0], h[2][1]); o1.y = pk2(h[2][2], h[2][3]); o1.z = pk2(h[3][0], h[3][1]); o1.w = pk2(h[3][2], h[3][3]);
;                 v4u* up = (v4u*)(u + (size_t)m * D); up[lane] = o0; up[64 + lane] = o1;
	v_pk_mul_f32 v[118:119], v[86:87], v[86:87]
	v_pk_mul_f32 v[120:121], v[84:85], v[84:85]
	v_mul_f32_e32 v2, v92, v92
	v_pk_mov_b32 v[122:123], v[120:121], v[118:119] op_sel:[1,0]
	v_mov_b32_e32 v121, v119
	v_pk_add_f32 v[118:119], v[122:123], v[120:121]
	v_pk_mul_f32 v[120:121], v[90:91], v[90:91]
	v_pk_mul_f32 v[122:123], v[88:89], v[88:89]
	v_pk_add_f32 v[118:119], v[118:119], v[118:119] op_sel_hi:[0,1]
	v_pk_mov_b32 v[124:125], v[122:123], v[120:121] op_sel:[1,0]
	v_mov_b32_e32 v123, v121
	v_pk_add_f32 v[120:121], v[124:125], v[122:123]
	v_pk_fma_f32 v[122:123], v[92:93], v[92:93], v[2:3] op_sel_hi:[1,1,0]
	v_mul_f32_e32 v2, v94, v94
	v_pk_add_f32 v[120:121], v[120:121], v[120:121] op_sel_hi:[0,1]
	v_pk_fma_f32 v[124:125], v[94:95], v[94:95], v[2:3] op_sel_hi:[1,1,0]
	v_mul_f32_e32 v122, v96, v96
	v_mul_f32_e32 v124, v97, v97
	v_mul_f32_e32 v118, v98, v98
	v_mul_f32_e32 v120, v99, v99
	v_pk_add_f32 v[122:123], v[122:123], v[124:125]
	v_pk_add_f32 v[118:119], v[118:119], v[120:121]
	v_cvt_pk_bf16_f32 v124, v96, v97
	v_cvt_pk_bf16_f32 v125, v98, v99
	s_nop 0
	v_pk_add_f32 v[118:119], v[122:123], v[118:119]
	v_cvt_pk_bf16_f32 v123, v94, v95
	s_nop 0
	v_add_f32_e32 v2, v118, v119
	s_nop 1
	v_add_f32_dpp v2, v2, v2 quad_perm:[1,0,3,2] row_mask:0xf bank_mask:0xf bound_ctrl:1
	s_nop 1
	v_add_f32_dpp v2, v2, v2 quad_perm:[2,3,0,1] row_mask:0xf bank_mask:0xf bound_ctrl:1
	s_nop 1
	v_add_f32_dpp v2, v2, v2 row_half_mirror row_mask:0xf bank_mask:0xf bound_ctrl:1
	s_nop 1
	v_add_f32_dpp v2, v2, v2 row_mirror row_mask:0xf bank_mask:0xf bound_ctrl:1
	s_nop 0
	v_readlane_b32 s1, v2, 16
	v_readlane_b32 s9, v2, 48
	v_readlane_b32 s4, v2, 0
	v_readlane_b32 s5, v2, 32
	v_mov_b32_e32 v118, s1
	v_mov_b32_e32 v119, s9
	v_pk_add_f32 v[118:119], s[4:5], v[118:119]
	s_brev_b32 s1, 64
	v_add_f32_e32 v2, v118, v119
	v_fmamk_f32 v2, v2, 0x3a800000, v214
	s_mov_b64 s[4:5], 0
	v_add_co_u32_e32 v126, vcc, s1, v116
	v_rsq_f32_e32 v2, v2
	s_nop 0
	v_cvt_pk_bf16_f32 v118, v84, v85
	v_cvt_pk_bf16_f32 v119, v86, v87
	v_cvt_pk_bf16_f32 v120, v88, v89
	v_cvt_pk_bf16_f32 v121, v90, v91
	v_cvt_pk_bf16_f32 v122, v92, v93
	s_nop 0
	v_addc_co_u32_e32 v127, vcc, 0, v117, vcc
	global_store_dwordx4 v[126:127], v[118:121], off sc1
	global_store_dwordx4 v[126:127], v[122:125], off offset:1024 sc1
	v_pk_mul_f32 v[126:127], v[92:93], v[2:3] op_sel_hi:[1,0]
	v_pk_mul_f32 v[118:119], v[84:85], v[2:3] op_sel_hi:[1,0]
	v_pk_mul_f32 v[120:121], v[86:87], v[2:3] op_sel_hi:[1,0]
	v_pk_mul_f32 v[122:123], v[88:89], v[2:3] op_sel_hi:[1,0]
	v_pk_mul_f32 v[120:121], v[26:27], v[120:121]
	v_pk_mul_f32 v[118:119], v[24:25], v[118:119]
	v_pk_mul_f32 v[122:123], v[20:21], v[122:123]
	v_pk_mul_f32 v[126:127], v[32:33], v[126:127]
	v_pk_mul_f32 v[124:125], v[90:91], v[2:3] op_sel_hi:[1,0]
	v_cvt_pk_bf16_f32 v118, v118, v119
	v_cvt_pk_bf16_f32 v119, v120, v121
	v_cvt_pk_bf16_f32 v120, v122, v123
	v_cvt_pk_bf16_f32 v122, v126, v127
	v_add_co_u32_e32 v126, vcc, 0xb000000, v114
	v_pk_mul_f32 v[124:125], v[22:23], v[124:125]
	v_pk_mul_f32 v[128:129], v[94:95], v[2:3] op_sel_hi:[1,0]
	v_pk_mul_f32 v[130:131], v[96:97], v[2:3] op_sel_hi:[1,0]
	v_pk_mul_f32 v[132:133], v[98:99], v[2:3] op_sel_hi:[1,0]
	v_cvt_pk_bf16_f32 v121, v124, v125
	v_addc_co_u32_e32 v127, vcc, 0, v115, vcc
	v_pk_mul_f32 v[128:129], v[34:35], v[128:129]
	v_pk_mul_f32 v[132:133], v[30:31], v[132:133]
	v_pk_mul_f32 v[130:131], v[28:29], v[130:131]
	v_cvt_pk_bf16_f32 v123, v128, v129
	v_cvt_pk_bf16_f32 v125, v132, v133
	s_nop 0
	v_cvt_pk_bf16_f32 v124, v130, v131
	flat_store_dwordx4 v[126:127], v[118:121] sc1
	flat_store_dwordx4 v[126:127], v[122:125] offset:1024 sc1

; __device__ __forceinline__ void thin_pass(const Ctx& C, const bf16* hin, bf16* hout, bf16* u, float* out, const bf16* y, const float* gpost, float cmul, const float* gpre, bool last) {
;     ...
;     for (int m0 = mstart; m0 < mend; m0 += mstep) {
;         v4u yr[RB][2], hr[RB][2];
; #pragma unroll
;         for (int b = 0; b < RB; ++b) { const v4u* yp = (const v4u*)(y + (size_t)(m0 + b) * D); const v4u* hp = (const v4u*)(hin + (size_t)(m0 + b) * D);
;             yr[b][0] = yp[lane]; yr[b][1] = yp[64 + lane]; hr[b][0] = hp[lane]; hr[b][1] = hp[64 + lane]; }
; #pragma unroll
;         for (int b = 0; b < RB; ++b) {
;             const int m = m0 + b; const v4u y0 = yr[b][0], y1 = yr[b][1], h0 = hr[b][0], h1 = hr[b][1];
;             f32x4 yv[4], h[4];
;             yv[0] = (f32x4){bf_lo(y0.x), bf_hi(y0.x), bf_lo(y0.y), bf_hi(y0.y)}; yv[1] = (f32x4){bf_lo(y0.z), bf_hi(y0.z), bf_lo(y0.w), bf_hi(y0.w)};
;             yv[2] = (f32x4){bf_lo(y1.x), bf_hi(y1.x), bf_lo(y1.y), bf_hi(y1.y)}; yv[3] = (f32x4){bf_lo(y1.z), bf_hi(y1.z), bf_lo(y1.w), bf_hi(y1.w)};
;             h[0] = (f32x4){bf_lo(h0.x), bf_hi(h0.x), bf_lo(h0.y), bf_hi(h0.y)}; h[1] = (f32x4){bf_lo(h0.z), bf_hi(h0.z), bf_lo(h0.w), bf_hi(h0.w)};
;             h[2] = (f32x4){bf_lo(h1.x), bf_hi(h1.x), bf_lo(h1.y), bf_hi(h1.y)}; h[3] = (f32x4){bf_lo(h1.z), bf_hi(h1.z), bf_lo(h1.w), bf_hi(h1.w)};
;             float ss = 0.f;
; #pragma unroll
;             for (int i = 0; i < 4; ++i) ss += (yv[i][0] * yv[i][0] + yv[i][1] * yv[i][1]) + (yv[i][2] * yv[i][2] + yv[i][3] * yv[i][3]);
;             const float ry = cmul / sqrtf(wave_sum(ss) * (1.0f / D) + RMS_EPS);
; #pragma unroll
;             for (int i = 0; i < 4; ++i) h[i] = h[i] + yv[i] * ry * g4[i];
.LBB0_1757:
	v_lshl_add_u64 v[102:103], s[8:9], 0, v[92:93]
	v_add_co_u32_e32 v36, vcc, 0xd000000, v102
	v_lshl_add_u64 v[38:39], s[14:15], 0, v[92:93]
	s_nop 0
	v_addc_co_u32_e32 v37, vcc, 0, v103, vcc
	flat_load_dwordx4 v[84:87], v[36:37] nt
	flat_load_dwordx4 v[88:91], v[36:37] offset:1024 nt
	v_add_co_u32_e32 v40, vcc, 0x2000000, v38
	s_add_i32 s2, s6, 3
	s_nop 0
	v_addc_co_u32_e32 v41, vcc, 0, v39, vcc
	global_load_dwordx4 v[104:107], v[40:41], off nt
	global_load_dwordx4 v[108:111], v[40:41], off offset:1024 nt
	flat_load_dwordx4 v[72:75], v[36:37] offset:2048 nt
	flat_load_dwordx4 v[68:71], v[36:37] offset:3072 nt
	global_load_dwordx4 v[80:83], v[40:41], off offset:2048 nt
	global_load_dwordx4 v[76:79], v[40:41], off offset:3072 nt
	s_ashr_i32 s3, s2, 31
	v_add_co_u32_e32 v36, vcc, s91, v102
	s_lshl_b64 s[16:17], s[2:3], 11
	s_nop 0
	v_addc_co_u32_e32 v37, vcc, 0, v103, vcc
	flat_load_dwordx4 v[56:59], v[36:37] nt
	flat_load_dwordx4 v[52:55], v[36:37] offset:1024 nt
	v_add_co_u32_e32 v36, vcc, s93, v38
	v_lshl_add_u64 v[44:45], v[96:97], 0, s[16:17]
	s_nop 0
	v_addc_co_u32_e32 v37, vcc, 0, v39, vcc
	global_load_dwordx4 v[64:67], v[36:37], off nt
	global_load_dwordx4 v[60:63], v[36:37], off offset:1024 nt
	v_lshl_add_u64 v[36:37], v[94:95], 0, s[16:17]
	flat_load_dwordx4 v[40:43], v[36:37] nt
	s_nop 0
	flat_load_dwordx4 v[36:39], v[36:37] offset:1024 nt
	s_nop 0
	global_load_dwordx4 v[48:51], v[44:45], off nt
	s_nop 0
	global_load_dwordx4 v[44:47], v[44:45], off offset:1024 nt
	s_add_i32 s6, s6, s4
	s_add_u32 s8, s8, s10
	s_addc_u32 s9, s9, s11
	s_waitcnt vmcnt(0) lgkmcnt(0)
	v_lshlrev_b32_e32 v129, 16, v87
	v_lshlrev_b32_e32 v128, 16, v86
	v_lshlrev_b32_e32 v114, 16, v106
	v_and_b32_e32 v115, 0xffff0000, v106
	v_lshlrev_b32_e32 v106, 16, v84
	v_lshlrev_b32_e32 v118, 16, v107
	v_and_b32_e32 v119, 0xffff0000, v107
	v_and_b32_e32 v107, 0xffff0000, v84
	v_mul_f32_e32 v2, v106, v106
	v_lshlrev_b32_e32 v84, 16, v85
	v_lshlrev_b32_e32 v120, 16, v108
	v_and_b32_e32 v121, 0xffff0000, v108
	v_lshlrev_b32_e32 v122, 16, v109
	v_and_b32_e32 v123, 0xffff0000, v109
	v_pk_fma_f32 v[108:109], v[106:107], v[106:107], v[2:3] op_sel_hi:[1,1,0]
	v_and_b32_e32 v85, 0xffff0000, v85
	v_mul_f32_e32 v2, v84, v84
	v_and_b32_e32 v87, 0xffff0000, v87
	v_and_b32_e32 v86, 0xffff0000, v86
	v_lshlrev_b32_e32 v132, 16, v88
	v_lshlrev_b32_e32 v116, 16, v90
	v_lshlrev_b32_e32 v124, 16, v110
	v_and_b32_e32 v125, 0xffff0000, v110
	v_lshlrev_b32_e32 v126, 16, v111
	v_and_b32_e32 v127, 0xffff0000, v111
	v_pk_fma_f32 v[110:111], v[84:85], v[84:85], v[2:3] op_sel_hi:[1,1,0]
	v_pk_mul_f32 v[130:131], v[86:87], v[86:87]
	v_and_b32_e32 v133, 0xffff0000, v88
	v_mul_f32_e32 v2, v132, v132
	v_lshlrev_b32_e32 v88, 16, v89
	v_pk_fma_f32 v[130:131], v[128:129], v[128:129], v[130:131]
	v_pk_fma_f32 v[134:135], v[132:133], v[132:133], v[2:3] op_sel_hi:[1,1,0]
	v_and_b32_e32 v89, 0xffff0000, v89
	v_mul_f32_e32 v2, v88, v88
	v_mov_b32_e32 v117, v109
	v_mov_b32_e32 v138, v116
	v_mov_b32_e32 v139, v111
	v_and_b32_e32 v140, 0xffff0000, v90
	v_lshlrev_b32_e32 v90, 16, v91
	v_and_b32_e32 v91, 0xffff0000, v91
	v_pk_add_f32 v[130:131], v[130:131], v[130:131] op_sel_hi:[0,1]
	v_pk_fma_f32 v[136:137], v[88:89], v[88:89], v[2:3] op_sel_hi:[1,1,0]
	v_pk_mul_f32 v[138:139], v[116:117], v[138:139]
	v_pk_add_f32 v[108:109], v[108:109], v[110:111]
	v_mul_f32_e32 v130, v140, v140
	v_mul_f32_e32 v134, v90, v90
	v_mul_f32_e32 v136, v91, v91
	v_mov_b32_e32 v139, v109
	v_pk_add_f32 v[108:109], v[138:139], v[130:131]
	v_pk_add_f32 v[110:111], v[134:135], v[136:137]
	v_lshlrev_b32_e32 v112, 16, v104
	v_pk_add_f32 v[108:109], v[108:109], v[110:111]
	v_and_b32_e32 v113, 0xffff0000, v104
	v_add_f32_e32 v2, v108, v109
	v_lshlrev_b32_e32 v104, 16, v105
	v_and_b32_e32 v105, 0xffff0000, v105
	v_add_f32_dpp v2, v2, v2 quad_perm:[1,0,3,2] row_mask:0xf bank_mask:0xf bound_ctrl:1
	s_nop 1
	v_add_f32_dpp v2, v2, v2 quad_perm:[2,3,0,1] row_mask:0xf bank_mask:0xf bound_ctrl:1
	s_nop 1
	v_add_f32_dpp v2, v2, v2 row_half_mirror row_mask:0xf bank_mask:0xf bound_ctrl:1
	s_nop 1
	v_add_f32_dpp v2, v2, v2 row_mirror row_mask:0xf bank_mask:0xf bound_ctrl:1
	s_nop 0
	v_readlane_b32 s5, v2, 16
	v_readlane_b32 s7, v2, 48
	v_readlane_b32 s2, v2, 0
	v_readlane_b32 s3, v2, 32
	v_mov_b32_e32 v108, s5
	v_mov_b32_e32 v109, s7
	v_pk_add_f32 v[108:109], s[2:3], v[108:109]
	s_nop 0
	v_add_f32_e32 v2, v108, v109
	v_fmamk_f32 v2, v2, 0x3a800000, v214
	v_rsq_f32_e32 v2, v2
	s_nop 0
	v_pk_mul_f32 v[84:85], v[2:3], v[84:85] op_sel_hi:[0,1]
	v_pk_fma_f32 v[104:105], v[10:11], v[84:85], v[104:105]
	v_mov_b32_e32 v84, v128
	v_mov_b32_e32 v85, v86
	v_mov_b32_e32 v86, v129
	v_pk_mul_f32 v[106:107], v[2:3], v[106:107] op_sel_hi:[0,1]
	v_pk_mul_f32 v[84:85], v[2:3], v[84:85] op_sel_hi:[0,1]
	v_pk_mul_f32 v[86:87], v[2:3], v[86:87] op_sel_hi:[0,1]
	v_pk_fma_f32 v[106:107], v[8:9], v[106:107], v[112:113]
	v_pk_fma_f32 v[108:109], v[6:7], v[86:87], v[118:119]
	v_pk_fma_f32 v[112:113], v[4:5], v[84:85], v[114:115]
	v_pk_mul_f32 v[84:85], v[2:3], v[132:133] op_sel_hi:[0,1]
	v_pk_mul_f32 v[86:87], v[2:3], v[88:89] op_sel_hi:[0,1]
	v_mov_b32_e32 v117, v140
	v_pk_fma_f32 v[110:111], v[18:19], v[86:87], v[122:123]
	v_pk_fma_f32 v[114:115], v[16:17], v[84:85], v[120:121]
	v_pk_mul_f32 v[84:85], v[90:91], v[2:3] op_sel_hi:[1,0]
	v_pk_mul_f32 v[86:87], v[116:117], v[2:3] op_sel_hi:[1,0]
	v_pk_fma_f32 v[118:119], v[14:15], v[84:85], v[126:127]
	v_pk_fma_f32 v[116:117], v[12:13], v[86:87], v[124:125]
	v_pk_mul_f32 v[84:85], v[104:105], v[104:105]
	v_pk_mul_f32 v[86:87], v[106:107], v[106:107]
	v_mul_f32_e32 v2, v114, v114
	v_pk_mov_b32 v[88:89], v[86:87], v[84:85] op_sel:[1,0]
; __device__ __forceinline__ void thin_pass(const Ctx& C, const bf16* hin, bf16* hout, bf16* u, float* out, const bf16* y, const float* gpost, float cmul, const float* gpre, bool last) {
;     ...
;             const int m = m0 + b; const v4u y0 = yr[b][0], y1 = yr[b][1], h0 = hr[b][0], h1 = hr[b][1];
;             f32x4 yv[4], h[4];
;             yv[0] = (f32x4){bf_lo(y0.x), bf_hi(y0.x), bf_lo(y0.y), bf_hi(y0.y)}; yv[1] = (f32x4){bf_lo(y0.z), bf_hi(y0.z), bf_lo(y0.w), bf_hi(y0.w)};
;             yv[2] = (f32x4){bf_lo(y1.x), bf_hi(y1.x), bf_lo(y1.y), bf_hi(y1.y)}; yv[3] = (f32x4){bf_lo(y1.z), bf_hi(y1.z), bf_lo(y1.w), bf_hi(y1.w)};
;             h[0] = (f32x4){bf_lo(h0.x), bf_hi(h0.x), bf_lo(h0.y), bf_hi(h0.y)}; h[1] = (f32x4){bf_lo(h0.z), bf_hi(h0.z), bf_lo(h0.w), bf_hi(h0.w)};
;             h[2] = (f32x4){bf_lo(h1.x), bf_hi(h1.x), bf_lo(h1.y), bf_hi(h1.y)}; h[3] = (f32x4){bf_lo(h1.z), bf_hi(h1.z), bf_lo(h1.w), bf_hi(h1.w)};
;             float ss = 0.f;
; #pragma unroll
;             for (int i = 0; i < 4; ++i) ss += (yv[i][0] * yv[i][0] + yv[i][1] * yv[i][1]) + (yv[i][2] * yv[i][2] + yv[i][3] * yv[i][3]);
;             const float ry = cmul / sqrtf(wave_sum(ss) * (1.0f / D) + RMS_EPS);
;     ...
;                 float s2 = 0.f;
; #pragma unroll
;                 for (int i = 0; i < 4; ++i) s2 += (h[i][0] * h[i][0] + h[i][1] * h[i][1]) + (h[i][2] * h[i][2] + h[i][3] * h[i][3]);
;                 const float rh = 1.0f / sqrtf(wave_sum(s2) * (1.0f / D) + RMS_EPS);
;                 v4u o0, o1; o0.x = pk2(h[0][0], h[0][1]); o0.y = pk2(h[0][2], h[0][3]); o0.z = pk2(h[1][0], h[1][1]); o0.w = pk2(h[1][2], h[1][3]);
;                 o1.x = pk2(h[2][0], h[2][1]); o1.y = pk2(h[2][2], h[2][3]); o1.z = pk2(h[3][0], h[3][1]); o1.w = pk2(h[3][2], h[3][3]);
;                 v4u* hp = (v4u*)(hout + (size_t)m * D); hp[lane] = o0; hp[64 + lane] = o1;
; #pragma unroll
;                 for (int i = 0; i < 4; ++i) h[i] = h[i] * rh * q4[i];
;                 o0.x = pk2(h[0][0], h[0][1]); o0.y = pk2(h[0][2], h[0][3]); o0.z = pk2(h[1][0], h[1][1]); o0.w = pk2(h[1][2], h[1][3]);
;                 o1.x = pk2(h[2][0], h[2][1]); o1.y = pk2(h[2][2], h[2][3]); o1.z = pk2(h[3][0], h[3][1]); o1.w = pk2(h[3][2], h[3][3]);
;                 v4u* up = (v4u*)(u + (size_t)m * D); up[lane] = o0; up[64 + lane] = o1;
	v_mov_b32_e32 v87, v85
	v_pk_add_f32 v[84:85], v[88:89], v[86:87]
	v_pk_mul_f32 v[86:87], v[108:109], v[108:109]
	v_pk_mul_f32 v[88:89], v[112:113], v[112:113]
	v_pk_add_f32 v[84:85], v[84:85], v[84:85] op_sel_hi:[0,1]
	v_pk_mov_b32 v[90:91], v[88:89], v[86:87] op_sel:[1,0]
	v_mov_b32_e32 v89, v87
	v_pk_add_f32 v[86:87], v[90:91], v[88:89]
	v_pk_fma_f32 v[88:89], v[114:115], v[114:115], v[2:3] op_sel_hi:[1,1,0]
	v_mul_f32_e32 v2, v110, v110
	v_pk_add_f32 v[86:87], v[86:87], v[86:87] op_sel_hi:[0,1]
	v_pk_fma_f32 v[90:91], v[110:111], v[110:111], v[2:3] op_sel_hi:[1,1,0]
	v_mul_f32_e32 v88, v116, v116
	v_mul_f32_e32 v90, v117, v117
	v_mul_f32_e32 v84, v118, v118
	v_mul_f32_e32 v86, v119, v119
	v_pk_add_f32 v[88:89], v[88:89], v[90:91]
	v_pk_add_f32 v[84:85], v[84:85], v[86:87]
	v_cvt_pk_bf16_f32 v90, v116, v117
	v_cvt_pk_bf16_f32 v91, v118, v119
	v_lshl_add_u64 v[120:121], s[12:13], 0, v[92:93]
	v_pk_add_f32 v[84:85], v[88:89], v[84:85]
	v_cvt_pk_bf16_f32 v89, v110, v111
	v_and_b32_e32 v128, 0xffff0000, v70
	v_add_f32_e32 v2, v84, v85
	s_add_u32 s12, s12, s10
	s_addc_u32 s13, s13, s11
	v_add_f32_dpp v2, v2, v2 quad_perm:[1,0,3,2] row_mask:0xf bank_mask:0xf bound_ctrl:1
	s_add_u32 s14, s14, s10
	s_addc_u32 s15, s15, s11
	v_add_f32_dpp v2, v2, v2 quad_perm:[2,3,0,1] row_mask:0xf bank_mask:0xf bound_ctrl:1
	s_cmp_lt_i32 s6, s1
	s_nop 0
	v_add_f32_dpp v2, v2, v2 row_half_mirror row_mask:0xf bank_mask:0xf bound_ctrl:1
	s_nop 1
	v_add_f32_dpp v2, v2, v2 row_mirror row_mask:0xf bank_mask:0xf bound_ctrl:1
	s_nop 0
	v_readlane_b32 s5, v2, 16
	v_readlane_b32 s7, v2, 48
	v_readlane_b32 s2, v2, 0
	v_readlane_b32 s3, v2, 32
	v_mov_b32_e32 v84, s5
	v_mov_b32_e32 v85, s7
	v_pk_add_f32 v[84:85], s[2:3], v[84:85]
	s_nop 0
	v_add_f32_e32 v2, v84, v85
	v_fmamk_f32 v2, v2, 0x3a800000, v214
	s_mov_b32 s2, 0xb000000
	v_rsq_f32_e32 v2, v2
	s_nop 0
	v_cvt_pk_bf16_f32 v84, v106, v107
	v_cvt_pk_bf16_f32 v85, v104, v105
	v_cvt_pk_bf16_f32 v86, v112, v113
	v_cvt_pk_bf16_f32 v87, v108, v109
	v_cvt_pk_bf16_f32 v88, v114, v115
	flat_store_dwordx4 v[120:121], v[84:87] sc1
	flat_store_dwordx4 v[120:121], v[88:91] offset:1024 sc1
	s_nop 0
	v_pk_mul_f32 v[84:85], v[106:107], v[2:3] op_sel_hi:[1,0]
	v_pk_mul_f32 v[86:87], v[104:105], v[2:3] op_sel_hi:[1,0]
	v_pk_mul_f32 v[90:91], v[108:109], v[2:3] op_sel_hi:[1,0]
	v_pk_mul_f32 v[108:109], v[116:117], v[2:3] op_sel_hi:[1,0]
	v_pk_mul_f32 v[86:87], v[26:27], v[86:87]
	v_pk_mul_f32 v[84:85], v[24:25], v[84:85]
	v_pk_mul_f32 v[88:89], v[112:113], v[2:3] op_sel_hi:[1,0]
	v_pk_mul_f32 v[90:91], v[22:23], v[90:91]
	v_pk_mul_f32 v[104:105], v[114:115], v[2:3] op_sel_hi:[1,0]
	v_pk_mul_f32 v[108:109], v[28:29], v[108:109]
	v_pk_mul_f32 v[88:89], v[20:21], v[88:89]
	v_pk_mul_f32 v[106:107], v[110:111], v[2:3] op_sel_hi:[1,0]
	v_pk_mul_f32 v[104:105], v[32:33], v[104:105]
	v_pk_mul_f32 v[110:111], v[118:119], v[2:3] op_sel_hi:[1,0]
	v_cvt_pk_bf16_f32 v84, v84, v85
	v_cvt_pk_bf16_f32 v85, v86, v87
	v_cvt_pk_bf16_f32 v87, v90, v91
	v_cvt_pk_bf16_f32 v90, v108, v109
	v_lshlrev_b32_e32 v108, 16, v72
	v_pk_mul_f32 v[110:111], v[30:31], v[110:111]
	v_cvt_pk_bf16_f32 v86, v88, v89
	v_cvt_pk_bf16_f32 v88, v104, v105
	v_add_co_u32_e32 v104, vcc, s2, v102
	v_and_b32_e32 v109, 0xffff0000, v72
	v_mul_f32_e32 v2, v108, v108
	v_lshlrev_b32_e32 v72, 16, v73
	v_cvt_pk_bf16_f32 v91, v110, v111
	v_addc_co_u32_e32 v105, vcc, 0, v103, vcc
	v_pk_fma_f32 v[110:111], v[108:109], v[108:109], v[2:3] op_sel_hi:[1,1,0]
	v_and_b32_e32 v73, 0xffff0000, v73
	v_mul_f32_e32 v2, v72, v72
	v_lshlrev_b32_e32 v115, 16, v75
	v_lshlrev_b32_e32 v114, 16, v74
	v_and_b32_e32 v75, 0xffff0000, v75
	v_and_b32_e32 v74, 0xffff0000, v74
	v_lshlrev_b32_e32 v118, 16, v68
	v_pk_mul_f32 v[106:107], v[34:35], v[106:107]
	v_pk_fma_f32 v[112:113], v[72:73], v[72:73], v[2:3] op_sel_hi:[1,1,0]
	v_cvt_pk_bf16_f32 v89, v106, v107
	flat_store_dwordx4 v[104:105], v[84:87] sc1
	flat_store_dwordx4 v[104:105], v[88:91] offset:1024 sc1
	v_pk_mul_f32 v[116:117], v[74:75], v[74:75]
	v_lshlrev_b32_e32 v84, 16, v70
	v_and_b32_e32 v119, 0xffff0000, v68
	v_mul_f32_e32 v2, v118, v118
	v_lshlrev_b32_e32 v68, 16, v69
	v_pk_fma_f32 v[116:117], v[114:115], v[114:115], v[116:117]
	v_pk_fma_f32 v[122:123], v[118:119], v[118:119], v[2:3] op_sel_hi:[1,1,0]
	v_and_b32_e32 v69, 0xffff0000, v69
	v_mul_f32_e32 v2, v68, v68
	v_mov_b32_e32 v85, v111
	v_mov_b32_e32 v126, v84
	v_mov_b32_e32 v127, v113
	v_lshlrev_b32_e32 v70, 16, v71
	v_and_b32_e32 v71, 0xffff0000, v71
	v_pk_add_f32 v[116:117], v[116:117], v[116:117] op_sel_hi:[0,1]
	v_pk_fma_f32 v[124:125], v[68:69], v[68:69], v[2:3] op_sel_hi:[1,1,0]
	v_pk_mul_f32 v[126:127], v[84:85], v[126:127]
	v_pk_add_f32 v[110:111], v[110:111], v[112:113]
	v_mul_f32_e32 v116, v128, v128
	v_mul_f32_e32 v122, v70, v70
	v_mul_f32_e32 v124, v71, v71
	v_mov_b32_e32 v127, v111
	v_pk_add_f32 v[110:111], v[126:127], v[116:117]
	v_pk_add_f32 v[112:113], v[122:123], v[124:125]
	v_lshlrev_b32_e32 v86, 16, v80
	v_pk_add_f32 v[110:111], v[110:111], v[112:113]
	v_and_b32_e32 v87, 0xffff0000, v80
	v_add_f32_e32 v2, v110, v111
	v_lshlrev_b32_e32 v80, 16, v81
	v_and_b32_e32 v81, 0xffff0000, v81
	v_add_f32_dpp v2, v2, v2 quad_perm:[1,0,3,2] row_mask:0xf bank_mask:0xf bound_ctrl:1
	v_lshlrev_b32_e32 v90, 16, v76
	v_and_b32_e32 v91, 0xffff0000, v76
	v_add_f32_dpp v2, v2, v2 quad_perm:[2,3,0,1] row_mask:0xf bank_mask:0xf bound_ctrl:1
	v_lshlrev_b32_e32 v76, 16, v77
	v_and_b32_e32 v77, 0xffff0000, v77
	v_add_f32_dpp v2, v2, v2 row_half_mirror row_mask:0xf bank_mask:0xf bound_ctrl:1
	v_lshlrev_b32_e32 v88, 16, v82
	v_and_b32_e32 v89, 0xffff0000, v82
	v_add_f32_dpp v2, v2, v2 row_mirror row_mask:0xf bank_mask:0xf bound_ctrl:1
; __device__ __forceinline__ void thin_pass(const Ctx& C, const bf16* hin, bf16* hout, bf16* u, float* out, const bf16* y, const float* gpost, float cmul, const float* gpre, bool last) {
;     ...
;             const int m = m0 + b; const v4u y0 = yr[b][0], y1 = yr[b][1], h0 = hr[b][0], h1 = hr[b][1];
;             f32x4 yv[4], h[4];
;             yv[0] = (f32x4){bf_lo(y0.x), bf_hi(y0.x), bf_lo(y0.y), bf_hi(y0.y)}; yv[1] = (f32x4){bf_lo(y0.z), bf_hi(y0.z), bf_lo(y0.w), bf_hi(y0.w)};
;             yv[2] = (f32x4){bf_lo(y1.x), bf_hi(y1.x), bf_lo(y1.y), bf_hi(y1.y)}; yv[3] = (f32x4){bf_lo(y1.z), bf_hi(y1.z), bf_lo(y1.w), bf_hi(y1.w)};
;             h[0] = (f32x4){bf_lo(h0.x), bf_hi(h0.x), bf_lo(h0.y), bf_hi(h0.y)}; h[1] = (f32x4){bf_lo(h0.z), bf_hi(h0.z), bf_lo(h0.w), bf_hi(h0.w)};
;             h[2] = (f32x4){bf_lo(h1.x), bf_hi(h1.x), bf_lo(h1.y), bf_hi(h1.y)}; h[3] = (f32x4){bf_lo(h1.z), bf_hi(h1.z), bf_lo(h1.w), bf_hi(h1.w)};
;             float ss = 0.f;
; #pragma unroll
;             for (int i = 0; i < 4; ++i) ss += (yv[i][0] * yv[i][0] + yv[i][1] * yv[i][1]) + (yv[i][2] * yv[i][2] + yv[i][3] * yv[i][3]);
;             const float ry = cmul / sqrtf(wave_sum(ss) * (1.0f / D) + RMS_EPS);
; #pragma unroll
;             for (int i = 0; i < 4; ++i) h[i] = h[i] + yv[i] * ry * g4[i];
;             if (last) { f32x4* op = (f32x4*)(out + (size_t)m * D); op[2 * lane] = h[0]; op[2 * lane + 1] = h[1]; op[128 + 2 * lane] = h[2]; op[128 + 2 * lane + 1] = h[3]; }
;             else {
;                 float s2 = 0.f;
; #pragma unroll
;                 for (int i = 0; i < 4; ++i) s2 += (h[i][0] * h[i][0] + h[i][1] * h[i][1]) + (h[i][2] * h[i][2] + h[i][3] * h[i][3]);
;                 const float rh = 1.0f / sqrtf(wave_sum(s2) * (1.0f / D) + RMS_EPS);
;                 v4u o0, o1; o0.x = pk2(h[0][0], h[0][1]); o0.y = pk2(h[0][2], h[0][3]); o0.z = pk2(h[1][0], h[1][1]); o0.w = pk2(h[1][2], h[1][3]);
;                 o1.x = pk2(h[2][0], h[2][1]); o1.y = pk2(h[2][2], h[2][3]); o1.z = pk2(h[3][0], h[3][1]); o1.w = pk2(h[3][2], h[3][3]);
;                 v4u* hp = (v4u*)(hout + (size_t)m * D); hp[lane] = o0; hp[64 + lane] = o1;
; #pragma unroll
;                 for (int i = 0; i < 4; ++i) h[i] = h[i] * rh * q4[i];
;                 o0.x = pk2(h[0][0], h[0][1]); o0.y = pk2(h[0][2], h[0][3]); o0.z = pk2(h[1][0], h[1][1]); o0.w = pk2(h[1][2], h[1][3]);
	v_lshlrev_b32_e32 v106, 16, v78
	v_readlane_b32 s5, v2, 16
	v_readlane_b32 s7, v2, 48
	v_readlane_b32 s2, v2, 0
	v_readlane_b32 s3, v2, 32
	v_mov_b32_e32 v110, s5
	v_mov_b32_e32 v111, s7
	v_pk_add_f32 v[110:111], s[2:3], v[110:111]
	v_and_b32_e32 v107, 0xffff0000, v78
	v_add_f32_e32 v2, v110, v111
	v_fmamk_f32 v2, v2, 0x3a800000, v214
	v_lshlrev_b32_e32 v78, 16, v79
	v_and_b32_e32 v79, 0xffff0000, v79
	v_lshlrev_b32_e32 v82, 16, v83
	v_and_b32_e32 v83, 0xffff0000, v83
	v_rsq_f32_e32 v2, v2
	s_nop 0
	v_pk_mul_f32 v[72:73], v[2:3], v[72:73] op_sel_hi:[0,1]
	v_pk_mul_f32 v[108:109], v[2:3], v[108:109] op_sel_hi:[0,1]
	v_pk_fma_f32 v[80:81], v[10:11], v[72:73], v[80:81]
	v_mov_b32_e32 v72, v114
	v_mov_b32_e32 v73, v74
	v_pk_mul_f32 v[68:69], v[2:3], v[68:69] op_sel_hi:[0,1]
	v_mov_b32_e32 v85, v128
	v_pk_fma_f32 v[86:87], v[8:9], v[108:109], v[86:87]
	v_pk_mul_f32 v[72:73], v[2:3], v[72:73] op_sel_hi:[0,1]
	v_mov_b32_e32 v74, v115
	v_pk_fma_f32 v[76:77], v[18:19], v[68:69], v[76:77]
	v_pk_mul_f32 v[68:69], v[70:71], v[2:3] op_sel_hi:[1,0]
	v_pk_mul_f32 v[70:71], v[84:85], v[2:3] op_sel_hi:[1,0]
	v_pk_mul_f32 v[74:75], v[2:3], v[74:75] op_sel_hi:[0,1]
	v_pk_fma_f32 v[88:89], v[4:5], v[72:73], v[88:89]
	v_pk_mul_f32 v[72:73], v[2:3], v[118:119] op_sel_hi:[0,1]
	v_pk_fma_f32 v[84:85], v[12:13], v[70:71], v[106:107]
	v_pk_fma_f32 v[78:79], v[14:15], v[68:69], v[78:79]
	v_pk_mul_f32 v[68:69], v[80:81], v[80:81]
	v_pk_mul_f32 v[70:71], v[86:87], v[86:87]
	v_pk_fma_f32 v[82:83], v[6:7], v[74:75], v[82:83]
	v_pk_fma_f32 v[90:91], v[16:17], v[72:73], v[90:91]
	v_pk_mov_b32 v[72:73], v[70:71], v[68:69] op_sel:[1,0]
	v_mov_b32_e32 v71, v69
	v_pk_add_f32 v[68:69], v[72:73], v[70:71]
	v_pk_mul_f32 v[70:71], v[82:83], v[82:83]
	v_pk_mul_f32 v[72:73], v[88:89], v[88:89]
	v_mul_f32_e32 v2, v90, v90
	v_pk_mov_b32 v[74:75], v[72:73], v[70:71] op_sel:[1,0]
	v_mov_b32_e32 v73, v71
	v_pk_add_f32 v[70:71], v[74:75], v[72:73]
	v_pk_fma_f32 v[72:73], v[90:91], v[90:91], v[2:3] op_sel_hi:[1,1,0]
	v_mul_f32_e32 v2, v76, v76
	v_pk_add_f32 v[68:69], v[68:69], v[68:69] op_sel_hi:[0,1]
	v_pk_add_f32 v[70:71], v[70:71], v[70:71] op_sel_hi:[0,1]
	v_pk_fma_f32 v[74:75], v[76:77], v[76:77], v[2:3] op_sel_hi:[1,1,0]
	v_mul_f32_e32 v72, v84, v84
	v_mul_f32_e32 v74, v85, v85
	v_mul_f32_e32 v68, v78, v78
	v_mul_f32_e32 v70, v79, v79
	v_pk_add_f32 v[72:73], v[72:73], v[74:75]
	v_pk_add_f32 v[68:69], v[68:69], v[70:71]
	v_cvt_pk_bf16_f32 v74, v84, v85
	v_cvt_pk_bf16_f32 v75, v78, v79
	v_and_b32_e32 v108, 0xffff0000, v54
	v_pk_add_f32 v[68:69], v[72:73], v[68:69]
	v_cvt_pk_bf16_f32 v73, v76, v77
	s_nop 0
	v_add_f32_e32 v2, v68, v69
	s_nop 1
	v_add_f32_dpp v2, v2, v2 quad_perm:[1,0,3,2] row_mask:0xf bank_mask:0xf bound_ctrl:1
	s_nop 1
	v_add_f32_dpp v2, v2, v2 quad_perm:[2,3,0,1] row_mask:0xf bank_mask:0xf bound_ctrl:1
	s_nop 1
	v_add_f32_dpp v2, v2, v2 row_half_mirror row_mask:0xf bank_mask:0xf bound_ctrl:1
	s_nop 1
	v_add_f32_dpp v2, v2, v2 row_mirror row_mask:0xf bank_mask:0xf bound_ctrl:1
	s_nop 0
	v_readlane_b32 s5, v2, 16
	v_readlane_b32 s7, v2, 48
	v_readlane_b32 s2, v2, 0
	v_readlane_b32 s3, v2, 32
	v_mov_b32_e32 v68, s5
	v_mov_b32_e32 v69, s7
	v_pk_add_f32 v[68:69], s[2:3], v[68:69]
	s_nop 0
	v_add_f32_e32 v2, v68, v69
	v_fmamk_f32 v2, v2, 0x3a800000, v214
	v_rsq_f32_e32 v2, v2
	s_nop 0
	v_cvt_pk_bf16_f32 v68, v86, v87
	v_cvt_pk_bf16_f32 v69, v80, v81
	v_cvt_pk_bf16_f32 v70, v88, v89
	v_cvt_pk_bf16_f32 v71, v82, v83
	v_cvt_pk_bf16_f32 v72, v90, v91
	flat_store_dwordx4 v[120:121], v[68:71] offset:2048 sc1
	flat_store_dwordx4 v[120:121], v[72:75] offset:3072 sc1
	v_pk_mul_f32 v[78:79], v[78:79], v[2:3] op_sel_hi:[1,0]
	v_pk_mul_f32 v[68:69], v[86:87], v[2:3] op_sel_hi:[1,0]
	v_pk_mul_f32 v[70:71], v[80:81], v[2:3] op_sel_hi:[1,0]
	v_pk_mul_f32 v[74:75], v[82:83], v[2:3] op_sel_hi:[1,0]
	v_pk_mul_f32 v[70:71], v[26:27], v[70:71]
	v_pk_mul_f32 v[68:69], v[24:25], v[68:69]
	v_pk_mul_f32 v[74:75], v[22:23], v[74:75]
	v_pk_mul_f32 v[78:79], v[30:31], v[78:79]
	v_pk_mul_f32 v[72:73], v[88:89], v[2:3] op_sel_hi:[1,0]
	v_pk_mul_f32 v[80:81], v[90:91], v[2:3] op_sel_hi:[1,0]
	v_cvt_pk_bf16_f32 v68, v68, v69
	v_cvt_pk_bf16_f32 v69, v70, v71
	v_cvt_pk_bf16_f32 v71, v74, v75
	v_cvt_pk_bf16_f32 v75, v78, v79
	v_lshlrev_b32_e32 v78, 16, v56
	v_pk_mul_f32 v[72:73], v[20:21], v[72:73]
	v_pk_mul_f32 v[76:77], v[76:77], v[2:3] op_sel_hi:[1,0]
	v_pk_mul_f32 v[80:81], v[32:33], v[80:81]
	v_pk_mul_f32 v[82:83], v[84:85], v[2:3] op_sel_hi:[1,0]
	v_and_b32_e32 v79, 0xffff0000, v56
	v_mul_f32_e32 v2, v78, v78
	v_lshlrev_b32_e32 v56, 16, v57
	v_pk_mul_f32 v[82:83], v[28:29], v[82:83]
	v_cvt_pk_bf16_f32 v70, v72, v73
	v_cvt_pk_bf16_f32 v72, v80, v81
	v_pk_fma_f32 v[80:81], v[78:79], v[78:79], v[2:3] op_sel_hi:[1,1,0]
	v_and_b32_e32 v57, 0xffff0000, v57
	v_mul_f32_e32 v2, v56, v56
	v_lshlrev_b32_e32 v85, 16, v59
	v_lshlrev_b32_e32 v84, 16, v58
	v_and_b32_e32 v59, 0xffff0000, v59
	v_and_b32_e32 v58, 0xffff0000, v58
	v_lshlrev_b32_e32 v88, 16, v52
	v_pk_mul_f32 v[76:77], v[34:35], v[76:77]
	v_cvt_pk_bf16_f32 v74, v82, v83
	v_pk_fma_f32 v[82:83], v[56:57], v[56:57], v[2:3] op_sel_hi:[1,1,0]
	v_cvt_pk_bf16_f32 v73, v76, v77
	flat_store_dwordx4 v[104:105], v[68:71] offset:2048 sc1
	flat_store_dwordx4 v[104:105], v[72:75] offset:3072 sc1
	v_pk_mul_f32 v[86:87], v[58:59], v[58:59]
	v_lshlrev_b32_e32 v68, 16, v54
	v_and_b32_e32 v89, 0xffff0000, v52
	v_mul_f32_e32 v2, v88, v88
	v_lshlrev_b32_e32 v52, 16, v53
	v_pk_fma_f32 v[86:87], v[84:85], v[84:85], v[86:87]
	v_pk_fma_f32 v[90:91], v[88:89], v[88:89], v[2:3] op_sel_hi:[1,1,0]
	v_and_b32_e32 v53, 0xffff0000, v53
	v_mul_f32_e32 v2, v52, v52
	v_mov_b32_e32 v69, v81
; __device__ __forceinline__ unsigned pk2(float lo, float hi) { unsigned r; asm("v_cvt_pk_bf16_f32 %0, %1, %2" : "=v"(r) : "v"(lo), "v"(hi)); return r; }
; __device__ __forceinline__ void thin_pass(const Ctx& C, const bf16* hin, bf16* hout, bf16* u, float* out, const bf16* y, const float* gpost, float cmul, const float* gpre, bool last) {
;     ...
;         for (int b = 0; b < RB; ++b) {
;             const int m = m0 + b; const v4u y0 = yr[b][0], y1 = yr[b][1], h0 = hr[b][0], h1 = hr[b][1];
;             f32x4 yv[4], h[4];
;             yv[0] = (f32x4){bf_lo(y0.x), bf_hi(y0.x), bf_lo(y0.y), bf_hi(y0.y)}; yv[1] = (f32x4){bf_lo(y0.z), bf_hi(y0.z), bf_lo(y0.w), bf_hi(y0.w)};
;             yv[2] = (f32x4){bf_lo(y1.x), bf_hi(y1.x), bf_lo(y1.y), bf_hi(y1.y)}; yv[3] = (f32x4){bf_lo(y1.z), bf_hi(y1.z), bf_lo(y1.w), bf_hi(y1.w)};
;             h[0] = (f32x4){bf_lo(h0.x), bf_hi(h0.x), bf_lo(h0.y), bf_hi(h0.y)}; h[1] = (f32x4){bf_lo(h0.z), bf_hi(h0.z), bf_lo(h0.w), bf_hi(h0.w)};
;             h[2] = (f32x4){bf_lo(h1.x), bf_hi(h1.x), bf_lo(h1.y), bf_hi(h1.y)}; h[3] = (f32x4){bf_lo(h1.z), bf_hi(h1.z), bf_lo(h1.w), bf_hi(h1.w)};
;             float ss = 0.f;
; #pragma unroll
;             for (int i = 0; i < 4; ++i) ss += (yv[i][0] * yv[i][0] + yv[i][1] * yv[i][1]) + (yv[i][2] * yv[i][2] + yv[i][3] * yv[i][3]);
;             const float ry = cmul / sqrtf(wave_sum(ss) * (1.0f / D) + RMS_EPS);
; #pragma unroll
;             for (int i = 0; i < 4; ++i) h[i] = h[i] + yv[i] * ry * g4[i];
;             if (last) { f32x4* op = (f32x4*)(out + (size_t)m * D); op[2 * lane] = h[0]; op[2 * lane + 1] = h[1]; op[128 + 2 * lane] = h[2]; op[128 + 2 * lane + 1] = h[3]; }
;             else {
;                 float s2 = 0.f;
; #pragma unroll
;                 for (int i = 0; i < 4; ++i) s2 += (h[i][0] * h[i][0] + h[i][1] * h[i][1]) + (h[i][2] * h[i][2] + h[i][3] * h[i][3]);
;                 const float rh = 1.0f / sqrtf(wave_sum(s2) * (1.0f / D) + RMS_EPS);
;                 v4u o0, o1; o0.x = pk2(h[0][0], h[0][1]); o0.y = pk2(h[0][2], h[0][3]); o0.z = pk2(h[1][0], h[1][1]); o0.w = pk2(h[1][2], h[1][3]);
;                 o1.x = pk2(h[2][0], h[2][1]); o1.y = pk2(h[2][2], h[2][3]); o1.z = pk2(h[3][0], h[3][1]); o1.w = pk2(h[3][2], h[3][3]);
;                 v4u* hp = (v4u*)(hout + (size_t)m * D); hp[lane] = o0; hp[64 + lane] = o1;
	v_mov_b32_e32 v106, v68
	v_mov_b32_e32 v107, v83
	v_lshlrev_b32_e32 v54, 16, v55
	v_and_b32_e32 v55, 0xffff0000, v55
	v_pk_add_f32 v[86:87], v[86:87], v[86:87] op_sel_hi:[0,1]
	v_pk_fma_f32 v[104:105], v[52:53], v[52:53], v[2:3] op_sel_hi:[1,1,0]
	v_pk_mul_f32 v[106:107], v[68:69], v[106:107]
	v_pk_add_f32 v[80:81], v[80:81], v[82:83]
	v_mul_f32_e32 v86, v108, v108
	v_mul_f32_e32 v90, v54, v54
	v_mul_f32_e32 v104, v55, v55
	v_mov_b32_e32 v107, v81
	v_pk_add_f32 v[80:81], v[106:107], v[86:87]
	v_pk_add_f32 v[82:83], v[90:91], v[104:105]
	v_lshlrev_b32_e32 v70, 16, v64
	v_pk_add_f32 v[80:81], v[80:81], v[82:83]
	v_and_b32_e32 v71, 0xffff0000, v64
	v_add_f32_e32 v2, v80, v81
	v_lshlrev_b32_e32 v64, 16, v65
	v_and_b32_e32 v65, 0xffff0000, v65
	v_add_f32_dpp v2, v2, v2 quad_perm:[1,0,3,2] row_mask:0xf bank_mask:0xf bound_ctrl:1
	v_lshlrev_b32_e32 v74, 16, v60
	v_and_b32_e32 v75, 0xffff0000, v60
	v_add_f32_dpp v2, v2, v2 quad_perm:[2,3,0,1] row_mask:0xf bank_mask:0xf bound_ctrl:1
	v_lshlrev_b32_e32 v60, 16, v61
	v_and_b32_e32 v61, 0xffff0000, v61
	v_add_f32_dpp v2, v2, v2 row_half_mirror row_mask:0xf bank_mask:0xf bound_ctrl:1
	v_lshlrev_b32_e32 v72, 16, v66
	v_and_b32_e32 v73, 0xffff0000, v66
	v_add_f32_dpp v2, v2, v2 row_mirror row_mask:0xf bank_mask:0xf bound_ctrl:1
	v_lshlrev_b32_e32 v76, 16, v62
	v_readlane_b32 s5, v2, 16
	v_readlane_b32 s7, v2, 48
	v_readlane_b32 s2, v2, 0
	v_readlane_b32 s3, v2, 32
	v_mov_b32_e32 v80, s5
	v_mov_b32_e32 v81, s7
	v_pk_add_f32 v[80:81], s[2:3], v[80:81]
	v_and_b32_e32 v77, 0xffff0000, v62
	v_add_f32_e32 v2, v80, v81
	v_fmamk_f32 v2, v2, 0x3a800000, v214
	v_lshlrev_b32_e32 v62, 16, v63
	v_and_b32_e32 v63, 0xffff0000, v63
	v_lshlrev_b32_e32 v66, 16, v67
	v_and_b32_e32 v67, 0xffff0000, v67
	v_rsq_f32_e32 v2, v2
	s_nop 0
	v_pk_mul_f32 v[56:57], v[2:3], v[56:57] op_sel_hi:[0,1]
	v_pk_mul_f32 v[78:79], v[2:3], v[78:79] op_sel_hi:[0,1]
	v_pk_fma_f32 v[64:65], v[10:11], v[56:57], v[64:65]
	v_mov_b32_e32 v56, v84
	v_mov_b32_e32 v57, v58
	v_pk_mul_f32 v[52:53], v[2:3], v[52:53] op_sel_hi:[0,1]
	v_mov_b32_e32 v69, v108
	v_pk_fma_f32 v[70:71], v[8:9], v[78:79], v[70:71]
	v_pk_mul_f32 v[56:57], v[2:3], v[56:57] op_sel_hi:[0,1]
	v_mov_b32_e32 v58, v85
	v_pk_fma_f32 v[60:61], v[18:19], v[52:53], v[60:61]
	v_pk_mul_f32 v[52:53], v[54:55], v[2:3] op_sel_hi:[1,0]
	v_pk_mul_f32 v[54:55], v[68:69], v[2:3] op_sel_hi:[1,0]
	v_pk_mul_f32 v[58:59], v[2:3], v[58:59] op_sel_hi:[0,1]
	v_pk_fma_f32 v[72:73], v[4:5], v[56:57], v[72:73]
	v_pk_mul_f32 v[56:57], v[2:3], v[88:89] op_sel_hi:[0,1]
	v_pk_fma_f32 v[68:69], v[12:13], v[54:55], v[76:77]
	v_pk_fma_f32 v[62:63], v[14:15], v[52:53], v[62:63]
	v_pk_mul_f32 v[52:53], v[64:65], v[64:65]
	v_pk_mul_f32 v[54:55], v[70:71], v[70:71]
	v_pk_fma_f32 v[66:67], v[6:7], v[58:59], v[66:67]
	v_pk_fma_f32 v[74:75], v[16:17], v[56:57], v[74:75]
	v_pk_mov_b32 v[56:57], v[54:55], v[52:53] op_sel:[1,0]
	v_mov_b32_e32 v55, v53
	v_pk_add_f32 v[52:53], v[56:57], v[54:55]
	v_pk_mul_f32 v[54:55], v[66:67], v[66:67]
	v_pk_mul_f32 v[56:57], v[72:73], v[72:73]
	v_mul_f32_e32 v2, v74, v74
	v_pk_mov_b32 v[58:59], v[56:57], v[54:55] op_sel:[1,0]
	v_mov_b32_e32 v57, v55
	v_pk_add_f32 v[54:55], v[58:59], v[56:57]
	v_pk_fma_f32 v[56:57], v[74:75], v[74:75], v[2:3] op_sel_hi:[1,1,0]
	v_mul_f32_e32 v2, v60, v60
	v_pk_add_f32 v[52:53], v[52:53], v[52:53] op_sel_hi:[0,1]
	v_pk_add_f32 v[54:55], v[54:55], v[54:55] op_sel_hi:[0,1]
	v_pk_fma_f32 v[58:59], v[60:61], v[60:61], v[2:3] op_sel_hi:[1,1,0]
	v_mul_f32_e32 v56, v68, v68
	v_mul_f32_e32 v58, v69, v69
	v_mul_f32_e32 v52, v62, v62
	v_mul_f32_e32 v54, v63, v63
	v_pk_add_f32 v[56:57], v[56:57], v[58:59]
	v_pk_add_f32 v[52:53], v[52:53], v[54:55]
	v_cvt_pk_bf16_f32 v58, v68, v69
	v_cvt_pk_bf16_f32 v59, v62, v63
	v_and_b32_e32 v80, 0xffff0000, v38
	v_pk_add_f32 v[52:53], v[56:57], v[52:53]
	v_cvt_pk_bf16_f32 v57, v60, v61
	s_nop 0
	v_add_f32_e32 v2, v52, v53
	s_nop 1
	v_add_f32_dpp v2, v2, v2 quad_perm:[1,0,3,2] row_mask:0xf bank_mask:0xf bound_ctrl:1
	s_nop 1
	v_add_f32_dpp v2, v2, v2 quad_perm:[2,3,0,1] row_mask:0xf bank_mask:0xf bound_ctrl:1
	s_nop 1
	v_add_f32_dpp v2, v2, v2 row_half_mirror row_mask:0xf bank_mask:0xf bound_ctrl:1
	s_nop 1
	v_add_f32_dpp v2, v2, v2 row_mirror row_mask:0xf bank_mask:0xf bound_ctrl:1
	s_nop 0
	v_readlane_b32 s5, v2, 16
	v_readlane_b32 s7, v2, 48
	v_readlane_b32 s2, v2, 0
	v_readlane_b32 s3, v2, 32
	v_mov_b32_e32 v52, s5
	v_mov_b32_e32 v53, s7
	v_pk_add_f32 v[52:53], s[2:3], v[52:53]
	s_nop 0
	v_add_f32_e32 v2, v52, v53
	v_fmamk_f32 v2, v2, 0x3a800000, v214
	s_mov_b32 s2, 0xb001000
	v_add_co_u32_e32 v76, vcc, s84, v120
	v_rsq_f32_e32 v2, v2
	s_nop 0
	v_cvt_pk_bf16_f32 v52, v70, v71
	v_cvt_pk_bf16_f32 v53, v64, v65
	v_cvt_pk_bf16_f32 v54, v72, v73
	v_cvt_pk_bf16_f32 v55, v66, v67
	s_nop 0
	v_addc_co_u32_e32 v77, vcc, 0, v121, vcc
	v_cvt_pk_bf16_f32 v56, v74, v75
	flat_store_dwordx4 v[76:77], v[52:55] sc1
	flat_store_dwordx4 v[76:77], v[56:59] offset:1024 sc1
	v_pk_mul_f32 v[62:63], v[62:63], v[2:3] op_sel_hi:[1,0]
	v_pk_mul_f32 v[52:53], v[70:71], v[2:3] op_sel_hi:[1,0]
	v_pk_mul_f32 v[54:55], v[64:65], v[2:3] op_sel_hi:[1,0]
	v_pk_mul_f32 v[58:59], v[66:67], v[2:3] op_sel_hi:[1,0]
	v_pk_mul_f32 v[54:55], v[26:27], v[54:55]
	v_pk_mul_f32 v[52:53], v[24:25], v[52:53]
	v_pk_mul_f32 v[56:57], v[72:73], v[2:3] op_sel_hi:[1,0]
	v_pk_mul_f32 v[58:59], v[22:23], v[58:59]
	v_pk_mul_f32 v[60:61], v[60:61], v[2:3] op_sel_hi:[1,0]
	v_pk_mul_f32 v[62:63], v[30:31], v[62:63]
	v_pk_mul_f32 v[56:57], v[20:21], v[56:57]
	v_pk_mul_f32 v[64:65], v[74:75], v[2:3] op_sel_hi:[1,0]
	v_pk_mul_f32 v[60:61], v[34:35], v[60:61]
	v_cvt_pk_bf16_f32 v52, v52, v53
; __device__ __forceinline__ unsigned pk2(float lo, float hi) { unsigned r; asm("v_cvt_pk_bf16_f32 %0, %1, %2" : "=v"(r) : "v"(lo), "v"(hi)); return r; }
; __device__ __forceinline__ void thin_pass(const Ctx& C, const bf16* hin, bf16* hout, bf16* u, float* out, const bf16* y, const float* gpost, float cmul, const float* gpre, bool last) {
;     ...
;         for (int b = 0; b < RB; ++b) {
;             const int m = m0 + b; const v4u y0 = yr[b][0], y1 = yr[b][1], h0 = hr[b][0], h1 = hr[b][1];
;             f32x4 yv[4], h[4];
;             yv[0] = (f32x4){bf_lo(y0.x), bf_hi(y0.x), bf_lo(y0.y), bf_hi(y0.y)}; yv[1] = (f32x4){bf_lo(y0.z), bf_hi(y0.z), bf_lo(y0.w), bf_hi(y0.w)};
;             yv[2] = (f32x4){bf_lo(y1.x), bf_hi(y1.x), bf_lo(y1.y), bf_hi(y1.y)}; yv[3] = (f32x4){bf_lo(y1.z), bf_hi(y1.z), bf_lo(y1.w), bf_hi(y1.w)};
;             h[0] = (f32x4){bf_lo(h0.x), bf_hi(h0.x), bf_lo(h0.y), bf_hi(h0.y)}; h[1] = (f32x4){bf_lo(h0.z), bf_hi(h0.z), bf_lo(h0.w), bf_hi(h0.w)};
;             h[2] = (f32x4){bf_lo(h1.x), bf_hi(h1.x), bf_lo(h1.y), bf_hi(h1.y)}; h[3] = (f32x4){bf_lo(h1.z), bf_hi(h1.z), bf_lo(h1.w), bf_hi(h1.w)};
;             float ss = 0.f;
; #pragma unroll
;             for (int i = 0; i < 4; ++i) ss += (yv[i][0] * yv[i][0] + yv[i][1] * yv[i][1]) + (yv[i][2] * yv[i][2] + yv[i][3] * yv[i][3]);
;             const float ry = cmul / sqrtf(wave_sum(ss) * (1.0f / D) + RMS_EPS);
; #pragma unroll
;             for (int i = 0; i < 4; ++i) h[i] = h[i] + yv[i] * ry * g4[i];
;     ...
; #pragma unroll
;                 for (int i = 0; i < 4; ++i) h[i] = h[i] * rh * q4[i];
;                 o0.x = pk2(h[0][0], h[0][1]); o0.y = pk2(h[0][2], h[0][3]); o0.z = pk2(h[1][0], h[1][1]); o0.w = pk2(h[1][2], h[1][3]);
;                 o1.x = pk2(h[2][0], h[2][1]); o1.y = pk2(h[2][2], h[2][3]); o1.z = pk2(h[3][0], h[3][1]); o1.w = pk2(h[3][2], h[3][3]);
;                 v4u* up = (v4u*)(u + (size_t)m * D); up[lane] = o0; up[64 + lane] = o1;
	v_cvt_pk_bf16_f32 v53, v54, v55
	v_cvt_pk_bf16_f32 v55, v58, v59
	v_cvt_pk_bf16_f32 v59, v62, v63
	v_lshlrev_b32_e32 v62, 16, v40
	v_pk_mul_f32 v[64:65], v[32:33], v[64:65]
	v_pk_mul_f32 v[66:67], v[68:69], v[2:3] op_sel_hi:[1,0]
	v_cvt_pk_bf16_f32 v54, v56, v57
	v_cvt_pk_bf16_f32 v57, v60, v61
	v_add_co_u32_e32 v60, vcc, s2, v102
	v_and_b32_e32 v63, 0xffff0000, v40
	v_mul_f32_e32 v2, v62, v62
	v_lshlrev_b32_e32 v40, 16, v41
	v_pk_mul_f32 v[66:67], v[28:29], v[66:67]
	v_cvt_pk_bf16_f32 v56, v64, v65
	v_addc_co_u32_e32 v61, vcc, 0, v103, vcc
	v_pk_fma_f32 v[64:65], v[62:63], v[62:63], v[2:3] op_sel_hi:[1,1,0]
	v_and_b32_e32 v41, 0xffff0000, v41
	v_mul_f32_e32 v2, v40, v40
	v_lshlrev_b32_e32 v69, 16, v43
	v_lshlrev_b32_e32 v68, 16, v42
	v_and_b32_e32 v43, 0xffff0000, v43
	v_and_b32_e32 v42, 0xffff0000, v42
	v_lshlrev_b32_e32 v72, 16, v36
	v_cvt_pk_bf16_f32 v58, v66, v67
	flat_store_dwordx4 v[60:61], v[52:55] sc1
	flat_store_dwordx4 v[60:61], v[56:59] offset:1024 sc1
	v_pk_fma_f32 v[66:67], v[40:41], v[40:41], v[2:3] op_sel_hi:[1,1,0]
	v_lshlrev_b32_e32 v52, 16, v38
	v_pk_mul_f32 v[70:71], v[42:43], v[42:43]
	v_and_b32_e32 v73, 0xffff0000, v36
	v_mul_f32_e32 v2, v72, v72
	v_lshlrev_b32_e32 v36, 16, v37
	v_pk_fma_f32 v[70:71], v[68:69], v[68:69], v[70:71]
	v_pk_fma_f32 v[74:75], v[72:73], v[72:73], v[2:3] op_sel_hi:[1,1,0]
	v_and_b32_e32 v37, 0xffff0000, v37
	v_mul_f32_e32 v2, v36, v36
	v_mov_b32_e32 v53, v65
	v_mov_b32_e32 v78, v52
	v_mov_b32_e32 v79, v67
	v_lshlrev_b32_e32 v38, 16, v39
	v_and_b32_e32 v39, 0xffff0000, v39
	v_pk_add_f32 v[70:71], v[70:71], v[70:71] op_sel_hi:[0,1]
	v_pk_fma_f32 v[76:77], v[36:37], v[36:37], v[2:3] op_sel_hi:[1,1,0]
	v_pk_mul_f32 v[78:79], v[52:53], v[78:79]
	v_pk_add_f32 v[64:65], v[64:65], v[66:67]
	v_mul_f32_e32 v70, v80, v80
	v_mul_f32_e32 v74, v38, v38
	v_mul_f32_e32 v76, v39, v39
	v_mov_b32_e32 v79, v65
	v_pk_add_f32 v[64:65], v[78:79], v[70:71]
	v_pk_add_f32 v[66:67], v[74:75], v[76:77]
	v_lshlrev_b32_e32 v54, 16, v48
	v_pk_add_f32 v[64:65], v[64:65], v[66:67]
	v_and_b32_e32 v55, 0xffff0000, v48
	v_add_f32_e32 v2, v64, v65
	v_lshlrev_b32_e32 v48, 16, v49
	v_and_b32_e32 v49, 0xffff0000, v49
	v_add_f32_dpp v2, v2, v2 quad_perm:[1,0,3,2] row_mask:0xf bank_mask:0xf bound_ctrl:1
	v_lshlrev_b32_e32 v58, 16, v44
	v_and_b32_e32 v59, 0xffff0000, v44
	v_add_f32_dpp v2, v2, v2 quad_perm:[2,3,0,1] row_mask:0xf bank_mask:0xf bound_ctrl:1
	v_lshlrev_b32_e32 v44, 16, v45
	v_and_b32_e32 v45, 0xffff0000, v45
	v_add_f32_dpp v2, v2, v2 row_half_mirror row_mask:0xf bank_mask:0xf bound_ctrl:1
	v_lshlrev_b32_e32 v56, 16, v50
	v_and_b32_e32 v57, 0xffff0000, v50
	v_add_f32_dpp v2, v2, v2 row_mirror row_mask:0xf bank_mask:0xf bound_ctrl:1
	v_lshlrev_b32_e32 v50, 16, v51
	v_readlane_b32 s5, v2, 16
	v_readlane_b32 s7, v2, 48
	v_readlane_b32 s2, v2, 0
	v_readlane_b32 s3, v2, 32
	v_mov_b32_e32 v64, s5
	v_mov_b32_e32 v65, s7
	v_pk_add_f32 v[64:65], s[2:3], v[64:65]
	v_and_b32_e32 v51, 0xffff0000, v51
	v_add_f32_e32 v2, v64, v65
	v_fmamk_f32 v2, v2, 0x3a800000, v214
	v_lshlrev_b32_e32 v60, 16, v46
	v_and_b32_e32 v61, 0xffff0000, v46
	v_lshlrev_b32_e32 v46, 16, v47
	v_and_b32_e32 v47, 0xffff0000, v47
	v_rsq_f32_e32 v2, v2
	s_nop 0
	v_pk_mul_f32 v[40:41], v[2:3], v[40:41] op_sel_hi:[0,1]
	v_pk_mul_f32 v[62:63], v[2:3], v[62:63] op_sel_hi:[0,1]
	v_pk_fma_f32 v[48:49], v[10:11], v[40:41], v[48:49]
	v_mov_b32_e32 v40, v69
	v_mov_b32_e32 v41, v43
	v_pk_mul_f32 v[36:37], v[2:3], v[36:37] op_sel_hi:[0,1]
	v_mov_b32_e32 v53, v80
	v_pk_fma_f32 v[54:55], v[8:9], v[62:63], v[54:55]
	v_pk_mul_f32 v[40:41], v[2:3], v[40:41] op_sel_hi:[0,1]
	v_mov_b32_e32 v69, v42
	v_pk_fma_f32 v[44:45], v[18:19], v[36:37], v[44:45]
	v_pk_mul_f32 v[36:37], v[38:39], v[2:3] op_sel_hi:[1,0]
; __device__ __forceinline__ unsigned pk2(float lo, float hi) { unsigned r; asm("v_cvt_pk_bf16_f32 %0, %1, %2" : "=v"(r) : "v"(lo), "v"(hi)); return r; }
; __device__ __forceinline__ void thin_pass(const Ctx& C, const bf16* hin, bf16* hout, bf16* u, float* out, const bf16* y, const float* gpost, float cmul, const float* gpre, bool last) {
;     ...
;                 float s2 = 0.f;
; #pragma unroll
;                 for (int i = 0; i < 4; ++i) s2 += (h[i][0] * h[i][0] + h[i][1] * h[i][1]) + (h[i][2] * h[i][2] + h[i][3] * h[i][3]);
;                 const float rh = 1.0f / sqrtf(wave_sum(s2) * (1.0f / D) + RMS_EPS);
;                 v4u o0, o1; o0.x = pk2(h[0][0], h[0][1]); o0.y = pk2(h[0][2], h[0][3]); o0.z = pk2(h[1][0], h[1][1]); o0.w = pk2(h[1][2], h[1][3]);
;                 o1.x = pk2(h[2][0], h[2][1]); o1.y = pk2(h[2][2], h[2][3]); o1.z = pk2(h[3][0], h[3][1]); o1.w = pk2(h[3][2], h[3][3]);
;                 v4u* hp = (v4u*)(hout + (size_t)m * D); hp[lane] = o0; hp[64 + lane] = o1;
; #pragma unroll
;                 for (int i = 0; i < 4; ++i) h[i] = h[i] * rh * q4[i];
;                 o0.x = pk2(h[0][0], h[0][1]); o0.y = pk2(h[0][2], h[0][3]); o0.z = pk2(h[1][0], h[1][1]); o0.w = pk2(h[1][2], h[1][3]);
;                 o1.x = pk2(h[2][0], h[2][1]); o1.y = pk2(h[2][2], h[2][3]); o1.z = pk2(h[3][0], h[3][1]); o1.w = pk2(h[3][2], h[3][3]);
;                 v4u* up = (v4u*)(u + (size_t)m * D); up[lane] = o0; up[64 + lane] = o1;
	v_pk_mul_f32 v[38:39], v[52:53], v[2:3] op_sel_hi:[1,0]
	v_pk_mul_f32 v[42:43], v[2:3], v[68:69] op_sel_hi:[0,1]
	v_pk_fma_f32 v[50:51], v[6:7], v[40:41], v[50:51]
	v_pk_mul_f32 v[40:41], v[2:3], v[72:73] op_sel_hi:[0,1]
	v_pk_fma_f32 v[52:53], v[12:13], v[38:39], v[60:61]
	v_pk_fma_f32 v[46:47], v[14:15], v[36:37], v[46:47]
	v_pk_mul_f32 v[36:37], v[48:49], v[48:49]
	v_pk_mul_f32 v[38:39], v[54:55], v[54:55]
	v_pk_fma_f32 v[56:57], v[4:5], v[42:43], v[56:57]
	v_pk_fma_f32 v[58:59], v[16:17], v[40:41], v[58:59]
	v_pk_mov_b32 v[40:41], v[38:39], v[36:37] op_sel:[1,0]
	v_mov_b32_e32 v39, v37
	v_pk_add_f32 v[36:37], v[40:41], v[38:39]
	v_pk_mul_f32 v[38:39], v[50:51], v[50:51]
	v_pk_mul_f32 v[40:41], v[56:57], v[56:57]
	v_mul_f32_e32 v2, v58, v58
	v_pk_mov_b32 v[42:43], v[40:41], v[38:39] op_sel:[1,0]
	v_mov_b32_e32 v41, v39
	v_pk_add_f32 v[38:39], v[42:43], v[40:41]
	v_pk_fma_f32 v[40:41], v[58:59], v[58:59], v[2:3] op_sel_hi:[1,1,0]
	v_mul_f32_e32 v2, v44, v44
	v_pk_add_f32 v[36:37], v[36:37], v[36:37] op_sel_hi:[0,1]
	v_pk_add_f32 v[38:39], v[38:39], v[38:39] op_sel_hi:[0,1]
	v_pk_fma_f32 v[42:43], v[44:45], v[44:45], v[2:3] op_sel_hi:[1,1,0]
	v_mul_f32_e32 v40, v52, v52
	v_mul_f32_e32 v42, v53, v53
	v_mul_f32_e32 v36, v46, v46
	v_mul_f32_e32 v38, v47, v47
	v_pk_add_f32 v[40:41], v[40:41], v[42:43]
	v_pk_add_f32 v[36:37], v[36:37], v[38:39]
	v_lshl_add_u64 v[60:61], v[98:99], 0, s[16:17]
	v_pk_add_f32 v[36:37], v[40:41], v[36:37]
	v_cvt_pk_bf16_f32 v41, v44, v45
	v_cvt_pk_bf16_f32 v42, v52, v53
	v_cvt_pk_bf16_f32 v43, v46, v47
	s_nop 0
	v_add_f32_e32 v2, v36, v37
	s_nop 1
	v_add_f32_dpp v2, v2, v2 quad_perm:[1,0,3,2] row_mask:0xf bank_mask:0xf bound_ctrl:1
	s_nop 1
	v_add_f32_dpp v2, v2, v2 quad_perm:[2,3,0,1] row_mask:0xf bank_mask:0xf bound_ctrl:1
	s_nop 1
	v_add_f32_dpp v2, v2, v2 row_half_mirror row_mask:0xf bank_mask:0xf bound_ctrl:1
	s_nop 1
	v_add_f32_dpp v2, v2, v2 row_mirror row_mask:0xf bank_mask:0xf bound_ctrl:1
	s_nop 0
	v_readlane_b32 s5, v2, 16
	v_readlane_b32 s7, v2, 48
	v_readlane_b32 s2, v2, 0
	v_readlane_b32 s3, v2, 32
	v_mov_b32_e32 v36, s5
	v_mov_b32_e32 v37, s7
	v_pk_add_f32 v[36:37], s[2:3], v[36:37]
	s_nop 0
	v_add_f32_e32 v2, v36, v37
	v_fmamk_f32 v2, v2, 0x3a800000, v214
	v_rsq_f32_e32 v2, v2
	s_nop 0
	v_cvt_pk_bf16_f32 v36, v54, v55
	v_cvt_pk_bf16_f32 v37, v48, v49
	v_cvt_pk_bf16_f32 v38, v56, v57
	v_cvt_pk_bf16_f32 v39, v50, v51
	v_cvt_pk_bf16_f32 v40, v58, v59
	flat_store_dwordx4 v[60:61], v[36:39] sc1
	flat_store_dwordx4 v[60:61], v[40:43] offset:1024 sc1
	v_pk_mul_f32 v[44:45], v[44:45], v[2:3] op_sel_hi:[1,0]
	v_pk_mul_f32 v[36:37], v[54:55], v[2:3] op_sel_hi:[1,0]
	v_pk_mul_f32 v[38:39], v[48:49], v[2:3] op_sel_hi:[1,0]
	v_pk_mul_f32 v[40:41], v[56:57], v[2:3] op_sel_hi:[1,0]
	v_pk_mul_f32 v[38:39], v[26:27], v[38:39]
	v_pk_mul_f32 v[36:37], v[24:25], v[36:37]
	v_pk_mul_f32 v[42:43], v[50:51], v[2:3] op_sel_hi:[1,0]
	v_pk_mul_f32 v[40:41], v[20:21], v[40:41]
	v_pk_mul_f32 v[44:45], v[34:35], v[44:45]
	v_pk_mul_f32 v[42:43], v[22:23], v[42:43]
	v_pk_mul_f32 v[48:49], v[58:59], v[2:3] op_sel_hi:[1,0]
	v_pk_mul_f32 v[50:51], v[52:53], v[2:3] op_sel_hi:[1,0]
	v_pk_mul_f32 v[46:47], v[46:47], v[2:3] op_sel_hi:[1,0]
	v_cvt_pk_bf16_f32 v36, v36, v37
	v_cvt_pk_bf16_f32 v37, v38, v39
	v_cvt_pk_bf16_f32 v38, v40, v41
	v_cvt_pk_bf16_f32 v39, v42, v43
	v_cvt_pk_bf16_f32 v41, v44, v45
	v_lshl_add_u64 v[44:45], v[100:101], 0, s[16:17]
	v_pk_mul_f32 v[48:49], v[32:33], v[48:49]
	v_pk_mul_f32 v[46:47], v[30:31], v[46:47]
	v_pk_mul_f32 v[50:51], v[28:29], v[50:51]
	v_cvt_pk_bf16_f32 v40, v48, v49
	v_cvt_pk_bf16_f32 v43, v46, v47
	s_nop 0
	v_cvt_pk_bf16_f32 v42, v50, v51
	flat_store_dwordx4 v[44:45], v[36:39] sc1
	flat_store_dwordx4 v[44:45], v[40:43] offset:1024 sc1
	s_cbranch_scc1 .LBB0_1757
